# sc1 write-through on layer kernels' 16B output stores (h16,h8,out) instead of plain/nt
# speedup vs baseline: 1.2678x; 1.2678x over previous
.LBB2_33:
	v_ashrrev_i32_e32 v55, 31, v54
	v_lshrrev_b32_e32 v19, 4, v65
	v_lshlrev_b64 v[20:21], 9, v[54:55]
	v_lshl_add_u64 v[20:21], s[16:17], 0, v[20:21]
	v_lshlrev_b32_e32 v24, 5, v19
	v_mov_b32_e32 v25, 0
	v_lshl_add_u64 v[20:21], v[20:21], 0, v[24:25]
	global_load_dwordx4 v[26:29], v[20:21], off
	global_load_dwordx4 v[30:33], v[20:21], off offset:16
	global_load_dwordx4 v[34:37], v[20:21], off offset:128
	global_load_dwordx4 v[38:41], v[20:21], off offset:144
	global_load_dwordx4 v[42:45], v[20:21], off offset:256
	global_load_dwordx4 v[46:49], v[20:21], off offset:272
	global_load_dwordx4 v[58:61], v[20:21], off offset:384
	s_nop 0
	global_load_dwordx4 v[20:23], v[20:21], off offset:400
	v_max_i32_e32 v24, 1, v67
	v_cvt_f32_u32_e32 v24, v24
	v_mul_f32_e32 v18, 0x43000000, v18
	v_pk_add_f32 v[2:3], v[2:3], v[18:19] op_sel_hi:[1,0] neg_lo:[0,1] neg_hi:[0,1]
	v_pk_add_f32 v[10:11], v[10:11], v[18:19] op_sel_hi:[1,0] neg_lo:[0,1] neg_hi:[0,1]
	v_pk_add_f32 v[4:5], v[4:5], v[18:19] op_sel_hi:[1,0] neg_lo:[0,1] neg_hi:[0,1]
	v_pk_add_f32 v[12:13], v[12:13], v[18:19] op_sel_hi:[1,0] neg_lo:[0,1] neg_hi:[0,1]
	v_pk_add_f32 v[6:7], v[6:7], v[18:19] op_sel_hi:[1,0] neg_lo:[0,1] neg_hi:[0,1]
	v_pk_add_f32 v[14:15], v[14:15], v[18:19] op_sel_hi:[1,0] neg_lo:[0,1] neg_hi:[0,1]
	v_pk_add_f32 v[8:9], v[8:9], v[18:19] op_sel_hi:[1,0] neg_lo:[0,1] neg_hi:[0,1]
	v_pk_add_f32 v[16:17], v[16:17], v[18:19] op_sel_hi:[1,0] neg_lo:[0,1] neg_hi:[0,1]
	v_div_scale_f32 v18, s[0:1], v24, v24, 1.0
	v_rcp_f32_e32 v51, v18
	v_mul_u32_u24_e32 v50, 0x110, v66
	v_add3_u32 v68, v77, v50, v78
	v_div_scale_f32 v50, vcc, 1.0, v24, 1.0
	v_fma_f32 v66, -v18, v51, 1.0
	v_fmac_f32_e32 v51, v66, v51
	v_mul_f32_e32 v66, v50, v51
	v_fma_f32 v67, -v18, v66, v50
	v_fmac_f32_e32 v66, v67, v51
	v_fma_f32 v18, -v18, v66, v50
	v_div_fmas_f32 v18, v18, v51, v66
	v_div_fixup_f32 v18, v18, v24, 1.0
	v_pk_mul_f32 v[2:3], v[18:19], v[2:3] op_sel_hi:[0,1]
	v_pk_mul_f32 v[10:11], v[18:19], v[10:11] op_sel_hi:[0,1]
	v_pk_mul_f32 v[4:5], v[18:19], v[4:5] op_sel_hi:[0,1]
	v_pk_mul_f32 v[50:51], v[18:19], v[6:7] op_sel_hi:[0,1]
	v_pk_mul_f32 v[66:67], v[18:19], v[8:9] op_sel_hi:[0,1]
	v_pk_mul_f32 v[12:13], v[18:19], v[12:13] op_sel_hi:[0,1]
	v_pk_mul_f32 v[14:15], v[18:19], v[14:15] op_sel_hi:[0,1]
	v_pk_mul_f32 v[16:17], v[18:19], v[16:17] op_sel_hi:[0,1]
	v_cvt_pk_f16_f32 v2, v2, v3
	v_cvt_pk_f16_f32 v6, v10, v11
	v_cvt_pk_f16_f32 v3, v4, v5
	v_cvt_pk_f16_f32 v4, v50, v51
	v_cvt_pk_f16_f32 v5, v66, v67
	v_cvt_pk_f16_f32 v7, v12, v13
	v_cvt_pk_f16_f32 v8, v14, v15
	v_cvt_pk_f16_f32 v9, v16, v17
	ds_write_b128 v68, v[2:5]
	ds_write_b128 v68, v[6:9] offset:16
	s_movk_i32 s10, 0x110
	v_lshl_add_u32 v50, v57, 9, 0
	v_and_b32_e32 v0, 48, v0
	s_waitcnt vmcnt(7)
	v_cvt_f16_f32_e32 v2, v26
	s_waitcnt vmcnt(6)
	v_cvt_f16_f32_e32 v6, v33
	v_cvt_pk_f16_f32 v4, v29, v30
	v_cvt_pk_f16_f32 v5, v31, v32
	s_waitcnt vmcnt(3)
	v_cvt_f16_f32_e32 v24, v42
	v_cvt_f16_f32_e32 v18, v41
	v_alignbit_b32 v16, v5, v4, 16
	v_alignbit_b32 v17, v6, v5, 16
	v_and_b32_e32 v5, 48, v65
	v_cvt_pk_f16_f32 v3, v27, v28
	v_cvt_f16_f32_e32 v9, v34
	v_cvt_pk_f16_f32 v26, v43, v44
	s_waitcnt vmcnt(2)
	v_cvt_f16_f32_e32 v28, v49
	s_waitcnt vmcnt(1)
	v_cvt_f16_f32_e32 v29, v58
	v_add_u32_e32 v5, 0, v5
	v_pack_b32_f16 v6, v24, v26
	v_add_u32_e32 v24, 0x10000, v5
	v_xor_b32_e32 v5, v19, v57
	v_cvt_pk_f16_f32 v7, v37, v38
	v_cvt_pk_f16_f32 v13, v39, v40
	v_lshlrev_b32_e32 v51, 4, v5
	v_cvt_pk_f16_f32 v10, v35, v36
	v_cvt_pk_f16_f32 v8, v45, v46
	v_cvt_pk_f16_f32 v27, v47, v48
	v_alignbit_b32 v15, v4, v3, 16
	v_alignbit_b32 v12, v13, v7, 16
	v_pack_b32_f16 v14, v2, v3
	v_alignbit_b32 v13, v18, v13, 16
	v_cvt_pk_f16_f32 v3, v59, v60
	v_add_u32_e32 v65, v50, v51
	v_mad_u32_u24 v18, v57, s10, v77
	v_xad_u32 v75, v51, 64, v50
	v_alignbit_b32 v11, v7, v10, 16
	v_alignbit_b32 v7, v8, v26, 16
	v_alignbit_b32 v8, v27, v8, 16
	v_pack_b32_f16 v10, v9, v10
	v_alignbit_b32 v9, v28, v27, 16
	v_pack_b32_f16 v2, v29, v3
	ds_read_b128 v[26:29], v24
	ds_read_b128 v[30:33], v65
	ds_read_b128 v[34:37], v65 offset:8192
	v_add_u32_e32 v74, v18, v0
	ds_read_b128 v[38:41], v75 offset:32768
	ds_read_b128 v[42:45], v74
	s_waitcnt vmcnt(0)
	v_cvt_pk_f16_f32 v4, v61, v20
	ds_read_b128 v[46:49], v24 offset:64
	ds_read_b128 v[58:61], v65 offset:16384
	s_waitcnt lgkmcnt(2)
	v_mfma_f32_16x16x32_f16 v[26:29], v[30:33], v[42:45], v[26:29]
	ds_read_b128 v[30:33], v24 offset:128
	ds_read_b128 v[66:69], v65 offset:24576
	v_cvt_pk_f16_f32 v0, v21, v22
	v_cvt_f16_f32_e32 v5, v23
	s_waitcnt lgkmcnt(3)
	v_mfma_f32_16x16x32_f16 v[34:37], v[34:37], v[42:45], v[46:49]
	ds_read_b128 v[20:23], v24 offset:192
	s_nop 1
	ds_read_b128 v[46:49], v65 offset:32768
	v_alignbit_b32 v3, v4, v3, 16
	v_alignbit_b32 v4, v0, v4, 16
	s_waitcnt lgkmcnt(3)
	v_mfma_f32_16x16x32_f16 v[30:33], v[58:61], v[42:45], v[30:33]
	ds_read_b128 v[58:61], v24 offset:256
	ds_read_b128 v[70:73], v65 offset:40960
	v_alignbit_b32 v5, v5, v0, 16
	v_lshlrev_b32_e32 v0, 2, v19
	s_waitcnt lgkmcnt(3)
	v_mfma_f32_16x16x32_f16 v[20:23], v[66:69], v[42:45], v[20:23]
	ds_read_b128 v[66:69], v24 offset:320
	ds_read_b128 v[78:81], v65 offset:49152
	s_waitcnt lgkmcnt(3)
	v_mfma_f32_16x16x32_f16 v[46:49], v[46:49], v[42:45], v[58:61]
	s_nop 2
	ds_read_b128 v[58:61], v24 offset:384
	ds_read_b128 v[82:85], v24 offset:448
	ds_read_b128 v[86:89], v65 offset:57344
	s_waitcnt lgkmcnt(4)
	v_mfma_f32_16x16x32_f16 v[66:69], v[70:73], v[42:45], v[66:69]
	ds_read_b128 v[70:73], v75 offset:8192
	ds_read_b128 v[90:93], v75 offset:16384
	ds_read_b128 v[94:97], v75 offset:24576
	s_waitcnt lgkmcnt(5)
	v_mfma_f32_16x16x32_f16 v[58:61], v[78:81], v[42:45], v[58:61]
	ds_read_b128 v[78:81], v75 offset:40960
	ds_read_b128 v[98:101], v75 offset:49152
	ds_read_b128 v[102:105], v75
	ds_read_b128 v[106:109], v75 offset:57344
	s_waitcnt lgkmcnt(7)
	v_mfma_f32_16x16x32_f16 v[42:45], v[86:89], v[42:45], v[82:85]
	s_nop 2
	ds_read_b128 v[82:85], v74 offset:64
	s_movk_i32 s0, 0x80
	v_xad_u32 v24, v51, s0, v50
	s_waitcnt lgkmcnt(0)
	v_mfma_f32_16x16x32_f16 v[26:29], v[102:105], v[82:85], v[26:29]
	v_mfma_f32_16x16x32_f16 v[34:37], v[70:73], v[82:85], v[34:37]
	v_mfma_f32_16x16x32_f16 v[30:33], v[90:93], v[82:85], v[30:33]
	v_mfma_f32_16x16x32_f16 v[20:23], v[94:97], v[82:85], v[20:23]
	v_mfma_f32_16x16x32_f16 v[38:41], v[38:41], v[82:85], v[46:49]
	s_nop 2
	ds_read_b128 v[46:49], v24 offset:32768
	v_mfma_f32_16x16x32_f16 v[66:69], v[78:81], v[82:85], v[66:69]
	ds_read_b128 v[70:73], v24 offset:8192
	ds_read_b128 v[78:81], v24 offset:16384
	ds_read_b128 v[86:89], v24 offset:24576
	v_mfma_f32_16x16x32_f16 v[58:61], v[98:101], v[82:85], v[58:61]
	ds_read_b128 v[90:93], v24 offset:40960
	ds_read_b128 v[94:97], v24 offset:49152
	ds_read_b128 v[98:101], v24
	ds_read_b128 v[102:105], v24 offset:57344
	v_mfma_f32_16x16x32_f16 v[42:45], v[106:109], v[82:85], v[42:45]
	ds_read_b128 v[82:85], v74 offset:128
	s_movk_i32 s0, 0xc0
	v_xad_u32 v50, v51, s0, v50
	s_waitcnt lgkmcnt(0)
	v_mfma_f32_16x16x32_f16 v[26:29], v[98:101], v[82:85], v[26:29]
	v_mfma_f32_16x16x32_f16 v[34:37], v[70:73], v[82:85], v[34:37]
	v_mfma_f32_16x16x32_f16 v[30:33], v[78:81], v[82:85], v[30:33]
	v_mfma_f32_16x16x32_f16 v[20:23], v[86:89], v[82:85], v[20:23]
	v_mfma_f32_16x16x32_f16 v[38:41], v[46:49], v[82:85], v[38:41]
	ds_read_b128 v[46:49], v50 offset:32768
	ds_read_b128 v[70:73], v50 offset:8192
	ds_read_b128 v[78:81], v50 offset:16384
	ds_read_b128 v[86:89], v50 offset:24576
	v_mfma_f32_16x16x32_f16 v[66:69], v[90:93], v[82:85], v[66:69]
	v_mfma_f32_16x16x32_f16 v[58:61], v[94:97], v[82:85], v[58:61]
	ds_read_b128 v[90:93], v50 offset:40960
	ds_read_b128 v[94:97], v50 offset:49152
	ds_read_b128 v[98:101], v50
	ds_read_b128 v[106:109], v50 offset:57344
	v_mfma_f32_16x16x32_f16 v[42:45], v[102:105], v[82:85], v[42:45]
	ds_read_b128 v[82:85], v74 offset:192
	s_waitcnt lgkmcnt(0)
	v_mfma_f32_16x16x32_f16 v[26:29], v[98:101], v[82:85], v[26:29]
	v_mfma_f32_16x16x32_f16 v[34:37], v[70:73], v[82:85], v[34:37]
	v_mfma_f32_16x16x32_f16 v[30:33], v[78:81], v[82:85], v[30:33]
	v_mfma_f32_16x16x32_f16 v[20:23], v[86:89], v[82:85], v[20:23]
	v_mfma_f32_16x16x32_f16 v[38:41], v[46:49], v[82:85], v[38:41]
	v_mfma_f32_16x16x32_f16 v[46:49], v[90:93], v[82:85], v[66:69]
	s_nop 2
	ds_read_b128 v[66:69], v65 offset:256
	ds_read_b128 v[70:73], v65 offset:8448
	ds_read_b128 v[78:81], v65 offset:16640
	ds_read_b128 v[86:89], v65 offset:24832
	v_mfma_f32_16x16x32_f16 v[58:61], v[94:97], v[82:85], v[58:61]
	ds_read_b128 v[90:93], v65 offset:33024
	ds_read_b128 v[94:97], v65 offset:41216
	ds_read_b128 v[98:101], v65 offset:49408
	ds_read_b128 v[102:105], v65 offset:57600
	v_mfma_f32_16x16x32_f16 v[42:45], v[106:109], v[82:85], v[42:45]
	s_waitcnt lgkmcnt(7)
	v_mfma_f32_16x16x32_f16 v[26:29], v[66:69], v[14:17], v[26:29]
	s_waitcnt lgkmcnt(6)
	v_mfma_f32_16x16x32_f16 v[34:37], v[70:73], v[14:17], v[34:37]
	s_waitcnt lgkmcnt(5)
	v_mfma_f32_16x16x32_f16 v[30:33], v[78:81], v[14:17], v[30:33]
	ds_read_b128 v[66:69], v75 offset:256
	ds_read_b128 v[70:73], v75 offset:8448
	ds_read_b128 v[78:81], v75 offset:16640
	ds_read_b128 v[82:85], v75 offset:24832
	s_waitcnt lgkmcnt(8)
	v_mfma_f32_16x16x32_f16 v[20:23], v[86:89], v[14:17], v[20:23]
	s_waitcnt lgkmcnt(7)
	v_mfma_f32_16x16x32_f16 v[38:41], v[90:93], v[14:17], v[38:41]
	s_waitcnt lgkmcnt(6)
	v_mfma_f32_16x16x32_f16 v[46:49], v[94:97], v[14:17], v[46:49]
	s_waitcnt lgkmcnt(5)
	v_mfma_f32_16x16x32_f16 v[58:61], v[98:101], v[14:17], v[58:61]
	ds_read_b128 v[86:89], v75 offset:33024
	ds_read_b128 v[90:93], v75 offset:41216
	ds_read_b128 v[94:97], v75 offset:49408
	ds_read_b128 v[98:101], v75 offset:57600
	s_waitcnt lgkmcnt(8)
	v_mfma_f32_16x16x32_f16 v[14:17], v[102:105], v[14:17], v[42:45]
	s_waitcnt lgkmcnt(7)
	v_mfma_f32_16x16x32_f16 v[26:29], v[66:69], v[10:13], v[26:29]
	s_waitcnt lgkmcnt(6)
	v_mfma_f32_16x16x32_f16 v[34:37], v[70:73], v[10:13], v[34:37]
	s_waitcnt lgkmcnt(5)
	v_mfma_f32_16x16x32_f16 v[30:33], v[78:81], v[10:13], v[30:33]
	s_waitcnt lgkmcnt(4)
	v_mfma_f32_16x16x32_f16 v[20:23], v[82:85], v[10:13], v[20:23]
	s_waitcnt lgkmcnt(3)
	v_mfma_f32_16x16x32_f16 v[38:41], v[86:89], v[10:13], v[38:41]
	s_waitcnt lgkmcnt(2)
	v_mfma_f32_16x16x32_f16 v[42:45], v[90:93], v[10:13], v[46:49]
	s_nop 2
	ds_read_b128 v[46:49], v24 offset:256
	ds_read_b128 v[66:69], v24 offset:8448
	ds_read_b128 v[70:73], v24 offset:16640
	ds_read_b128 v[78:81], v24 offset:24832
	s_waitcnt lgkmcnt(5)
	v_mfma_f32_16x16x32_f16 v[58:61], v[94:97], v[10:13], v[58:61]
	ds_read_b128 v[82:85], v24 offset:33024
	ds_read_b128 v[86:89], v24 offset:41216
	ds_read_b128 v[90:93], v24 offset:49408
	ds_read_b128 v[94:97], v24 offset:57600
	s_waitcnt lgkmcnt(8)
	v_mfma_f32_16x16x32_f16 v[10:13], v[98:101], v[10:13], v[14:17]
	s_waitcnt lgkmcnt(7)
	v_mfma_f32_16x16x32_f16 v[14:17], v[46:49], v[6:9], v[26:29]
	s_waitcnt lgkmcnt(6)
	v_mfma_f32_16x16x32_f16 v[26:29], v[66:69], v[6:9], v[34:37]
	s_waitcnt lgkmcnt(5)
	v_mfma_f32_16x16x32_f16 v[30:33], v[70:73], v[6:9], v[30:33]
	s_waitcnt lgkmcnt(4)
	v_mfma_f32_16x16x32_f16 v[20:23], v[78:81], v[6:9], v[20:23]
	s_waitcnt lgkmcnt(3)
	v_mfma_f32_16x16x32_f16 v[34:37], v[82:85], v[6:9], v[38:41]
	s_waitcnt lgkmcnt(2)
	v_mfma_f32_16x16x32_f16 v[38:41], v[86:89], v[6:9], v[42:45]
	s_nop 2
	ds_read_b128 v[42:45], v50 offset:256
	ds_read_b128 v[46:49], v50 offset:8448
	ds_read_b128 v[66:69], v50 offset:16640
	ds_read_b128 v[70:73], v50 offset:24832
	s_waitcnt lgkmcnt(5)
	v_mfma_f32_16x16x32_f16 v[58:61], v[90:93], v[6:9], v[58:61]
	ds_read_b128 v[78:81], v50 offset:33024
	ds_read_b128 v[82:85], v50 offset:41216
	ds_read_b128 v[86:89], v50 offset:49408
	ds_read_b128 v[90:93], v50 offset:57600
	s_waitcnt lgkmcnt(8)
	v_mfma_f32_16x16x32_f16 v[6:9], v[94:97], v[6:9], v[10:13]
	s_waitcnt lgkmcnt(7)
	v_mfma_f32_16x16x32_f16 v[10:13], v[42:45], v[2:5], v[14:17]
	s_waitcnt lgkmcnt(6)
	v_mfma_f32_16x16x32_f16 v[14:17], v[46:49], v[2:5], v[26:29]
	s_waitcnt lgkmcnt(5)
	v_mfma_f32_16x16x32_f16 v[26:29], v[66:69], v[2:5], v[30:33]
	s_waitcnt lgkmcnt(4)
	v_mfma_f32_16x16x32_f16 v[20:23], v[70:73], v[2:5], v[20:23]
	s_waitcnt lgkmcnt(3)
	v_mfma_f32_16x16x32_f16 v[30:33], v[78:81], v[2:5], v[34:37]
	s_waitcnt lgkmcnt(2)
	v_mfma_f32_16x16x32_f16 v[34:37], v[82:85], v[2:5], v[38:41]
	s_waitcnt lgkmcnt(1)
	v_mfma_f32_16x16x32_f16 v[38:41], v[86:89], v[2:5], v[58:61]
	s_waitcnt lgkmcnt(0)
	v_mfma_f32_16x16x32_f16 v[2:5], v[90:93], v[2:5], v[6:9]
	s_nop 2
	v_max_f32_e32 v7, v12, v12
	v_max_f32_e32 v44, 0, v7
	v_max_f32_e32 v7, v13, v13
	v_max_f32_e32 v45, 0, v7
	v_max_f32_e32 v7, v14, v14
	v_max_f32_e32 v46, 0, v7
	v_max_f32_e32 v7, v15, v15
	v_max_f32_e32 v47, 0, v7
	v_max_f32_e32 v7, v16, v16
	v_max_f32_e32 v48, 0, v7
	v_max_f32_e32 v7, v17, v17
	v_max_f32_e32 v49, 0, v7
	v_max_f32_e32 v7, v26, v26
	v_max_f32_e32 v26, 0, v7
	v_max_f32_e32 v7, v27, v27
	v_max_f32_e32 v27, 0, v7
	v_max_f32_e32 v7, v28, v28
	v_max_f32_e32 v28, 0, v7
	v_max_f32_e32 v7, v29, v29
	v_max_f32_e32 v29, 0, v7
	v_max_f32_e32 v7, v20, v20
	v_max_f32_e32 v6, v10, v10
	v_max_f32_e32 v20, 0, v7
	v_max_f32_e32 v7, v21, v21
	v_max_f32_e32 v42, 0, v6
	v_max_f32_e32 v6, v11, v11
	v_max_f32_e32 v21, 0, v7
	v_max_f32_e32 v7, v22, v22
	v_max_f32_e32 v43, 0, v6
	v_max_f32_e32 v22, 0, v7
	v_max_f32_e32 v7, v23, v23
	v_max_f32_e32 v6, v42, v43
	v_max_f32_e32 v23, 0, v7
	v_max_f32_e32 v7, v30, v30
	v_max3_f32 v6, v6, v44, v45
	v_max_f32_e32 v30, 0, v7
	v_max_f32_e32 v7, v31, v31
	v_max3_f32 v6, v6, v46, v47
	v_max_f32_e32 v31, 0, v7
	v_max_f32_e32 v7, v32, v32
	v_max3_f32 v6, v6, v48, v49
	v_max_f32_e32 v32, 0, v7
	v_max_f32_e32 v7, v33, v33
	v_max3_f32 v6, v6, v26, v27
	v_max_f32_e32 v33, 0, v7
	v_max_f32_e32 v7, v34, v34
	v_max3_f32 v6, v6, v28, v29
	v_max_f32_e32 v34, 0, v7
	v_max_f32_e32 v7, v35, v35
	v_max3_f32 v6, v6, v20, v21
	v_max_f32_e32 v35, 0, v7
	v_max_f32_e32 v7, v36, v36
	v_max3_f32 v6, v6, v22, v23
	v_max_f32_e32 v36, 0, v7
	v_max_f32_e32 v7, v37, v37
	v_max3_f32 v6, v6, v30, v31
	v_max_f32_e32 v37, 0, v7
	v_max_f32_e32 v7, v38, v38
	v_max3_f32 v6, v6, v32, v33
	v_max_f32_e32 v38, 0, v7
	v_max_f32_e32 v7, v39, v39
	v_max3_f32 v6, v6, v34, v35
	v_max_f32_e32 v39, 0, v7
	v_max_f32_e32 v7, v40, v40
	v_max_f32_e32 v2, v2, v2
	v_max3_f32 v6, v6, v36, v37
	v_max_f32_e32 v40, 0, v7
	v_max_f32_e32 v7, v41, v41
	v_max_f32_e32 v50, 0, v2
	v_max_f32_e32 v2, v3, v3
	v_max3_f32 v6, v6, v38, v39
	v_max_f32_e32 v41, 0, v7
	v_max_f32_e32 v3, 0, v2
	v_max_f32_e32 v2, v4, v4
	v_max3_f32 v6, v6, v40, v41
	v_max_f32_e32 v51, 0, v2
	v_max_f32_e32 v2, v5, v5
	v_max3_f32 v6, v6, v50, v3
	v_max_f32_e32 v2, 0, v2
	v_max3_f32 v4, v6, v51, v2
	ds_bpermute_b32 v1, v1, v4
	s_mov_b32 s10, 0x437f0000
	v_lshlrev_b32_e32 v24, 4, v57
	v_lshl_add_u64 v[12:13], s[4:5], 0, v[24:25]
	s_waitcnt lgkmcnt(0)
	v_max_f32_e32 v1, v1, v1
	v_max_f32_e32 v1, v4, v1
	ds_bpermute_b32 v4, v64, v1
	s_waitcnt lgkmcnt(0)
	v_max_f32_e32 v4, v4, v4
	v_max_f32_e32 v1, v1, v4
	v_div_scale_f32 v4, s[0:1], v1, v1, s10
	v_rcp_f32_e32 v5, v4
	s_nop 0
	v_fma_f32 v6, -v4, v5, 1.0
	v_fmac_f32_e32 v5, v6, v5
	v_div_scale_f32 v6, vcc, s10, v1, s10
	v_mul_f32_e32 v7, v6, v5
	v_fma_f32 v8, -v4, v7, v6
	v_fmac_f32_e32 v7, v8, v5
	v_fma_f32 v4, -v4, v7, v6
	v_div_fmas_f32 v4, v4, v5, v7
	v_div_fixup_f32 v58, v4, v1, s10
	v_lshl_add_u32 v8, v19, 3, v18
	v_cvt_pk_f16_f32 v5, v44, v45
	v_cvt_pk_f16_f32 v4, v42, v43
	v_cvt_pk_f16_f32 v7, v48, v49
	v_cvt_pk_f16_f32 v6, v46, v47
	ds_write2_b64 v8, v[4:5], v[6:7] offset1:4
	v_cvt_pk_f16_f32 v5, v28, v29
	v_cvt_pk_f16_f32 v4, v26, v27
	v_cvt_pk_f16_f32 v7, v22, v23
	v_cvt_pk_f16_f32 v6, v20, v21
	ds_write2_b64 v8, v[4:5], v[6:7] offset0:8 offset1:12
	v_cvt_pk_f16_f32 v5, v32, v33
	v_cvt_pk_f16_f32 v4, v30, v31
	v_cvt_pk_f16_f32 v7, v36, v37
	v_cvt_pk_f16_f32 v6, v34, v35
	ds_write2_b64 v8, v[4:5], v[6:7] offset0:16 offset1:20
	v_cvt_pk_f16_f32 v5, v40, v41
	v_cvt_pk_f16_f32 v4, v38, v39
	v_cvt_pk_f16_f32 v7, v51, v2
	v_cvt_pk_f16_f32 v6, v50, v3
	ds_write2_b64 v8, v[4:5], v[6:7] offset0:24 offset1:28
	v_or_b32_e32 v4, v19, v63
	v_lshlrev_b32_e32 v18, 2, v4
	ds_bpermute_b32 v8, v18, v52
	v_mul_u32_u24_e32 v4, 0x110, v19
	v_add3_u32 v19, v77, v24, v4
	ds_read_b128 v[4:7], v19
	v_or_b32_e32 v10, 16, v18
	ds_bpermute_b32 v14, v10, v52
	s_waitcnt lgkmcnt(2)
	v_ashrrev_i32_e32 v9, 31, v8
	v_lshlrev_b64 v[8:9], 8, v[8:9]
	v_lshl_add_u64 v[16:17], v[12:13], 0, v[8:9]
	ds_read_b128 v[8:11], v19 offset:1088
	s_waitcnt lgkmcnt(2)
	global_store_dwordx4 v[16:17], v[4:7], off sc1
	s_waitcnt lgkmcnt(1)
	v_ashrrev_i32_e32 v15, 31, v14
	v_cmp_lt_f32_e32 vcc, 0, v1
	v_or_b32_e32 v4, 32, v18
	ds_bpermute_b32 v16, v4, v52
	v_lshlrev_b64 v[4:5], 8, v[14:15]
	v_lshl_add_u64 v[4:5], v[12:13], 0, v[4:5]
	s_waitcnt lgkmcnt(1)
	global_store_dwordx4 v[4:5], v[8:11], off sc1
	ds_read_b128 v[4:7], v19 offset:2176
	s_waitcnt lgkmcnt(1)
	v_ashrrev_i32_e32 v17, 31, v16
	v_or_b32_e32 v8, 48, v18
	ds_bpermute_b32 v14, v8, v52
	v_lshlrev_b64 v[8:9], 8, v[16:17]
	v_lshl_add_u64 v[16:17], v[12:13], 0, v[8:9]
	ds_read_b128 v[8:11], v19 offset:3264
	s_waitcnt lgkmcnt(2)
	global_store_dwordx4 v[16:17], v[4:7], off sc1
	s_waitcnt lgkmcnt(1)
	v_ashrrev_i32_e32 v15, 31, v14
	v_lshlrev_b64 v[4:5], 8, v[14:15]
	v_lshl_add_u64 v[4:5], v[12:13], 0, v[4:5]
	s_waitcnt lgkmcnt(0)
	global_store_dwordx4 v[4:5], v[8:11], off sc1
	v_cndmask_b32_e32 v4, 0, v58, vcc
	v_mul_f32_e32 v5, v4, v42
	v_mul_f32_e32 v6, v4, v43
	v_rndne_f32_e32 v5, v5
	v_rndne_f32_e32 v6, v6
	v_mul_f32_e32 v7, v4, v44
	v_cvt_i32_f32_e32 v5, v5
	v_cvt_i32_f32_e32 v6, v6
	v_rndne_f32_e32 v7, v7
	v_cvt_i32_f32_e32 v7, v7
	v_mul_u32_u24_e32 v8, 0x90, v57
	v_lshl_or_b32 v5, v6, 8, v5
	v_add3_u32 v0, v77, v8, v0
	v_lshl_or_b32 v5, v7, 16, v5
	v_mul_f32_e32 v6, v4, v45
	v_mul_f32_e32 v7, v4, v46
	v_mul_f32_e32 v8, v4, v47
	v_rndne_f32_e32 v6, v6
	v_rndne_f32_e32 v7, v7
	v_rndne_f32_e32 v8, v8
	v_mul_f32_e32 v9, v4, v48
	v_cvt_i32_f32_e32 v6, v6
	v_cvt_i32_f32_e32 v7, v7
	v_cvt_i32_f32_e32 v8, v8
	v_rndne_f32_e32 v9, v9
	v_mul_f32_e32 v10, v4, v49
	v_cvt_i32_f32_e32 v9, v9
	v_rndne_f32_e32 v10, v10
	v_cvt_i32_f32_e32 v10, v10
	v_lshl_or_b32 v5, v6, 24, v5
	v_lshl_or_b32 v6, v8, 8, v7
	v_lshl_or_b32 v6, v9, 16, v6
	v_lshl_or_b32 v6, v10, 24, v6
	ds_write2_b32 v0, v5, v6 offset1:4
	v_mul_f32_e32 v5, v4, v26
	v_mul_f32_e32 v6, v4, v27
	v_rndne_f32_e32 v5, v5
	v_rndne_f32_e32 v6, v6
	v_mul_f32_e32 v7, v4, v28
	v_cvt_i32_f32_e32 v5, v5
	v_cvt_i32_f32_e32 v6, v6
	v_rndne_f32_e32 v7, v7
	v_mul_f32_e32 v8, v4, v29
	v_cvt_i32_f32_e32 v7, v7
	v_rndne_f32_e32 v8, v8
	v_cvt_i32_f32_e32 v8, v8
	v_mul_f32_e32 v9, v4, v20
	v_mul_f32_e32 v10, v4, v21
	v_rndne_f32_e32 v9, v9
	v_rndne_f32_e32 v10, v10
	v_lshl_or_b32 v5, v6, 8, v5
	v_cvt_i32_f32_e32 v9, v9
	v_cvt_i32_f32_e32 v10, v10
	v_lshl_or_b32 v5, v7, 16, v5
	v_mul_f32_e32 v7, v4, v22
	v_lshl_or_b32 v5, v8, 24, v5
	v_rndne_f32_e32 v7, v7
	v_mul_f32_e32 v8, v4, v23
	v_cvt_i32_f32_e32 v7, v7
	v_rndne_f32_e32 v8, v8
	v_cvt_i32_f32_e32 v8, v8
	v_lshl_or_b32 v6, v10, 8, v9
	v_mul_f32_e32 v9, v4, v30
	v_mul_f32_e32 v10, v4, v31
	v_rndne_f32_e32 v9, v9
	v_rndne_f32_e32 v10, v10
	v_cvt_i32_f32_e32 v9, v9
	v_cvt_i32_f32_e32 v10, v10
	v_lshl_or_b32 v6, v7, 16, v6
	v_lshl_or_b32 v6, v8, 24, v6
	ds_write2_b32 v0, v5, v6 offset0:8 offset1:12
	v_mul_f32_e32 v6, v4, v32
	v_rndne_f32_e32 v6, v6
	v_mul_f32_e32 v7, v4, v33
	v_lshl_or_b32 v5, v10, 8, v9
	v_cvt_i32_f32_e32 v6, v6
	v_rndne_f32_e32 v7, v7
	v_mul_f32_e32 v8, v4, v34
	v_mul_f32_e32 v9, v4, v35
	v_cvt_i32_f32_e32 v7, v7
	v_rndne_f32_e32 v8, v8
	v_rndne_f32_e32 v9, v9
	v_cvt_i32_f32_e32 v8, v8
	v_cvt_i32_f32_e32 v9, v9
	v_mul_f32_e32 v10, v4, v36
	v_lshl_or_b32 v5, v6, 16, v5
	v_rndne_f32_e32 v10, v10
	v_lshl_or_b32 v5, v7, 24, v5
	v_mul_f32_e32 v7, v4, v37
	v_cvt_i32_f32_e32 v10, v10
	v_lshl_or_b32 v6, v9, 8, v8
	v_rndne_f32_e32 v7, v7
	v_mul_f32_e32 v8, v4, v38
	v_mul_f32_e32 v9, v4, v39
	v_cvt_i32_f32_e32 v7, v7
	v_rndne_f32_e32 v8, v8
	v_rndne_f32_e32 v9, v9
	v_cvt_i32_f32_e32 v8, v8
	v_cvt_i32_f32_e32 v9, v9
	v_lshl_or_b32 v6, v10, 16, v6
	v_lshl_or_b32 v6, v7, 24, v6
	v_mul_f32_e32 v7, v4, v50
	v_mul_f32_e32 v3, v4, v3
	v_mul_f32_e32 v10, v4, v40
	ds_write2_b32 v0, v5, v6 offset0:16 offset1:20
	v_lshl_or_b32 v5, v9, 8, v8
	v_rndne_f32_e32 v7, v7
	v_rndne_f32_e32 v3, v3
	v_mul_f32_e32 v8, v4, v51
	v_rndne_f32_e32 v10, v10
	v_mul_f32_e32 v6, v4, v41
	v_cvt_i32_f32_e32 v7, v7
	v_cvt_i32_f32_e32 v3, v3
	v_rndne_f32_e32 v8, v8
	v_mul_f32_e32 v2, v4, v2
	v_cvt_i32_f32_e32 v10, v10
	v_rndne_f32_e32 v6, v6
	v_cvt_i32_f32_e32 v8, v8
	v_rndne_f32_e32 v2, v2
	v_cvt_i32_f32_e32 v6, v6
	v_cvt_i32_f32_e32 v2, v2
	v_lshl_or_b32 v3, v3, 8, v7
	v_lshl_or_b32 v5, v10, 16, v5
	v_lshl_or_b32 v3, v8, 16, v3
	v_lshl_or_b32 v4, v6, 24, v5
	v_lshl_or_b32 v2, v2, 24, v3
	ds_write2_b32 v0, v4, v2 offset0:24 offset1:28
	v_or_b32_e32 v0, v62, v63
	v_lshlrev_b32_e32 v0, 2, v0
	ds_bpermute_b32 v6, v0, v52
	v_or_b32_e32 v8, v53, v63
	v_mul_u32_u24_e32 v0, 0x90, v62
	v_lshlrev_b32_e32 v8, 2, v8
	v_add3_u32 v0, v77, v56, v0
	ds_bpermute_b32 v12, v8, v52
	v_mov_b32_e32 v57, v25
	ds_read_b128 v[2:5], v0
	s_waitcnt lgkmcnt(2)
	v_ashrrev_i32_e32 v7, 31, v6
	v_lshl_add_u64 v[10:11], s[6:7], 0, v[56:57]
	v_lshlrev_b64 v[6:7], 7, v[6:7]
	v_lshl_add_u64 v[14:15], v[10:11], 0, v[6:7]
	ds_read_b128 v[6:9], v0 offset:1152
	s_waitcnt lgkmcnt(2)
	v_ashrrev_i32_e32 v13, 31, v12
	s_waitcnt lgkmcnt(1)
	global_store_dwordx4 v[14:15], v[2:5], off sc1
	s_nop 1
	v_lshlrev_b64 v[2:3], 7, v[12:13]
	v_lshl_add_u64 v[2:3], v[10:11], 0, v[2:3]
	s_waitcnt lgkmcnt(0)
	global_store_dwordx4 v[2:3], v[6:9], off sc1
	s_and_b64 exec, exec, s[2:3]
	s_cbranch_execz .LBB2_35
	s_mov_b32 s0, 0x3b808081
	v_lshl_add_u64 v[2:3], v[54:55], 1, s[8:9]
	v_fma_mixlo_f16 v0, v1, s0, 0
	global_store_short v[2:3], v0, off
.LBB2_35:
	s_endpgm
	.p2alignl 8, 3212836864

.LBB3_33:
	v_mov_b32_e32 v18, v1
	v_max_i32_e32 v1, 1, v53
	v_cvt_f32_u32_e32 v1, v1
	v_mov_b32_e32 v32, v3
	v_mov_b32_e32 v19, v4
	v_mov_b32_e32 v28, v9
	v_div_scale_f32 v3, s[0:1], v1, v1, 1.0
	v_rcp_f32_e32 v4, v3
	v_mov_b32_e32 v33, v10
	v_mov_b32_e32 v34, v11
	v_mov_b32_e32 v35, v12
	v_fma_f32 v9, -v3, v4, 1.0
	v_fmac_f32_e32 v4, v9, v4
	v_div_scale_f32 v9, vcc, 1.0, v1, 1.0
	v_mul_f32_e32 v10, v9, v4
	v_fma_f32 v11, -v3, v10, v9
	v_fmac_f32_e32 v10, v11, v4
	v_fma_f32 v3, -v3, v10, v9
	v_div_fmas_f32 v3, v3, v4, v10
	v_div_fixup_f32 v12, v3, v1, 1.0
	v_fma_mixlo_f16 v30, v12, v2, 0
	v_pk_mul_f32 v[2:3], v[12:13], v[18:19] op_sel_hi:[0,1]
	v_ashrrev_i32_e32 v53, 31, v52
	v_cvt_pk_f16_f32 v37, v2, v3
	v_lshlrev_b64 v[2:3], 8, v[52:53]
	v_lshl_add_u64 v[2:3], s[10:11], 0, v[2:3]
	v_and_b32_e32 v24, 48, v17
	v_mov_b32_e32 v25, 0
	v_lshl_add_u64 v[26:27], v[2:3], 0, v[24:25]
	v_mov_b32_e32 v29, v16
	v_fma_mixlo_f16 v31, v12, v8, 0
	v_lshrrev_b32_e32 v1, 4, v17
	v_mov_b32_e32 v36, v5
	global_load_dwordx4 v[20:23], v[26:27], off
	global_load_dwordx4 v[16:19], v[26:27], off offset:64
	global_load_dwordx4 v[8:11], v[26:27], off offset:128
	global_load_dwordx4 v[2:5], v[26:27], off offset:192
	v_pk_mul_f32 v[28:29], v[12:13], v[28:29] op_sel_hi:[0,1]
	v_cvt_pk_f16_f32 v24, v28, v29
	v_pk_mul_f32 v[28:29], v[12:13], v[32:33] op_sel_hi:[0,1]
	v_cvt_pk_f16_f32 v32, v28, v29
	v_pack_b32_f16 v26, v30, v37
	v_alignbit_b32 v27, v32, v37, 16
	v_pk_mul_f32 v[28:29], v[12:13], v[34:35] op_sel_hi:[0,1]
	v_mov_b32_e32 v37, v6
	v_cvt_pk_f16_f32 v34, v28, v29
	v_pk_mul_f32 v[28:29], v[12:13], v[36:37] op_sel_hi:[0,1]
	v_cvt_pk_f16_f32 v6, v28, v29
	v_alignbit_b32 v28, v6, v32, 16
	v_mov_b32_e32 v32, v13
	v_mov_b32_e32 v33, v14
	v_pk_mul_f32 v[32:33], v[12:13], v[32:33] op_sel_hi:[0,1]
	v_lshrrev_b32_e32 v29, 16, v6
	v_cvt_pk_f16_f32 v6, v32, v33
	v_alignbit_b32 v32, v6, v34, 16
	v_lshrrev_b32_e32 v33, 16, v6
	v_mul_u32_u24_e32 v6, 0x110, v59
	v_pack_b32_f16 v30, v31, v24
	v_fma_mixhi_f16 v29, v12, v7, 0
	v_fma_mixhi_f16 v33, v12, v15, 0
	v_add3_u32 v6, v73, v6, v71
	v_xor_b32_e32 v12, v1, v51
	v_alignbit_b32 v31, v34, v24, 16
	ds_write_b128 v6, v[26:29]
	ds_write_b128 v6, v[30:33] offset:16
	v_and_b32_e32 v0, 48, v0
	v_lshl_add_u32 v7, v51, 9, 0
	v_lshlrev_b32_e32 v24, 4, v12
	v_mul_u32_u24_e32 v30, 0x110, v51
	v_add_u32_e32 v6, 0, v0
	v_add_u32_e32 v56, v7, v24
	v_add3_u32 v0, v73, v30, v0
	v_add_u32_e32 v6, 0x10000, v6
	ds_read_b128 v[12:15], v56
	ds_read_b128 v[26:29], v56 offset:8192
	ds_read_b128 v[30:33], v0
	ds_read_b128 v[34:37], v6
	ds_read_b128 v[38:41], v6 offset:64
	v_xad_u32 v57, v24, 64, v7
	ds_read_b128 v[42:45], v57 offset:32768
	s_waitcnt lgkmcnt(2)
	v_mfma_f32_16x16x32_f16 v[12:15], v[12:15], v[30:33], v[34:37]
	s_nop 2
	ds_read_b128 v[34:37], v56 offset:16384
	ds_read_b128 v[46:49], v56 offset:24576
	s_waitcnt lgkmcnt(3)
	v_mfma_f32_16x16x32_f16 v[26:29], v[26:29], v[30:33], v[38:41]
	s_nop 2
	ds_read_b128 v[38:41], v6 offset:128
	ds_read_b128 v[52:55], v6 offset:192
	s_waitcnt lgkmcnt(1)
	v_mfma_f32_16x16x32_f16 v[34:37], v[34:37], v[30:33], v[38:41]
	s_nop 2
	ds_read_b128 v[38:41], v56 offset:32768
	ds_read_b128 v[60:63], v56 offset:40960
	s_waitcnt lgkmcnt(2)
	v_mfma_f32_16x16x32_f16 v[46:49], v[46:49], v[30:33], v[52:55]
	s_nop 2
	ds_read_b128 v[52:55], v6 offset:256
	s_waitcnt vmcnt(8)
	ds_read_b128 v[64:67], v6 offset:320
	s_waitcnt vmcnt(4)
	ds_read_b128 v[68:71], v56 offset:49152
	s_waitcnt lgkmcnt(2)
	v_mfma_f32_16x16x32_f16 v[38:41], v[38:41], v[30:33], v[52:55]
	s_nop 2
	ds_read_b128 v[52:55], v6 offset:384
	ds_read_b128 v[74:77], v6 offset:448
	ds_read_b128 v[78:81], v56 offset:57344
	s_waitcnt lgkmcnt(4)
	v_mfma_f32_16x16x32_f16 v[60:63], v[60:63], v[30:33], v[64:67]
	s_nop 2
	ds_read_b128 v[64:67], v57 offset:8192
	ds_read_b128 v[82:85], v57 offset:16384
	ds_read_b128 v[86:89], v57 offset:24576
	s_waitcnt lgkmcnt(5)
	v_mfma_f32_16x16x32_f16 v[52:55], v[68:71], v[30:33], v[52:55]
	ds_read_b128 v[68:71], v57 offset:40960
	ds_read_b128 v[90:93], v57 offset:49152
	ds_read_b128 v[94:97], v57
	ds_read_b128 v[98:101], v57 offset:57344
	s_waitcnt lgkmcnt(7)
	v_mfma_f32_16x16x32_f16 v[30:33], v[78:81], v[30:33], v[74:77]
	s_nop 2
	ds_read_b128 v[74:77], v0 offset:64
	s_movk_i32 s0, 0x80
	v_xad_u32 v6, v24, s0, v7
	s_waitcnt lgkmcnt(0)
	v_mfma_f32_16x16x32_f16 v[12:15], v[94:97], v[74:77], v[12:15]
	v_mfma_f32_16x16x32_f16 v[26:29], v[64:67], v[74:77], v[26:29]
	v_mfma_f32_16x16x32_f16 v[34:37], v[82:85], v[74:77], v[34:37]
	v_mfma_f32_16x16x32_f16 v[46:49], v[86:89], v[74:77], v[46:49]
	v_mfma_f32_16x16x32_f16 v[38:41], v[42:45], v[74:77], v[38:41]
	ds_read_b128 v[42:45], v6 offset:32768
	v_mfma_f32_16x16x32_f16 v[60:63], v[68:71], v[74:77], v[60:63]
	ds_read_b128 v[64:67], v6 offset:8192
	ds_read_b128 v[68:71], v6 offset:16384
	ds_read_b128 v[78:81], v6 offset:24576
	v_mfma_f32_16x16x32_f16 v[52:55], v[90:93], v[74:77], v[52:55]
	ds_read_b128 v[82:85], v6 offset:40960
	ds_read_b128 v[86:89], v6 offset:49152
	ds_read_b128 v[90:93], v6
	ds_read_b128 v[94:97], v6 offset:57344
	v_mfma_f32_16x16x32_f16 v[30:33], v[98:101], v[74:77], v[30:33]
	ds_read_b128 v[74:77], v0 offset:128
	s_movk_i32 s0, 0xc0
	v_xad_u32 v7, v24, s0, v7
	s_waitcnt lgkmcnt(0)
	v_mfma_f32_16x16x32_f16 v[12:15], v[90:93], v[74:77], v[12:15]
	v_mfma_f32_16x16x32_f16 v[26:29], v[64:67], v[74:77], v[26:29]
	v_mfma_f32_16x16x32_f16 v[34:37], v[68:71], v[74:77], v[34:37]
	v_mfma_f32_16x16x32_f16 v[46:49], v[78:81], v[74:77], v[46:49]
	v_mfma_f32_16x16x32_f16 v[38:41], v[42:45], v[74:77], v[38:41]
	ds_read_b128 v[42:45], v7 offset:32768
	ds_read_b128 v[64:67], v7 offset:8192
	ds_read_b128 v[68:71], v7 offset:16384
	ds_read_b128 v[78:81], v7 offset:24576
	v_mfma_f32_16x16x32_f16 v[60:63], v[82:85], v[74:77], v[60:63]
	v_mfma_f32_16x16x32_f16 v[52:55], v[86:89], v[74:77], v[52:55]
	ds_read_b128 v[82:85], v7 offset:40960
	ds_read_b128 v[86:89], v7 offset:49152
	ds_read_b128 v[90:93], v7
	ds_read_b128 v[98:101], v7 offset:57344
	v_mfma_f32_16x16x32_f16 v[30:33], v[94:97], v[74:77], v[30:33]
	ds_read_b128 v[74:77], v0 offset:192
	s_waitcnt lgkmcnt(0)
	v_mfma_f32_16x16x32_f16 v[12:15], v[90:93], v[74:77], v[12:15]
	v_mfma_f32_16x16x32_f16 v[26:29], v[64:67], v[74:77], v[26:29]
	v_mfma_f32_16x16x32_f16 v[34:37], v[68:71], v[74:77], v[34:37]
	v_mfma_f32_16x16x32_f16 v[46:49], v[78:81], v[74:77], v[46:49]
	v_mfma_f32_16x16x32_f16 v[38:41], v[42:45], v[74:77], v[38:41]
	v_mfma_f32_16x16x32_f16 v[42:45], v[82:85], v[74:77], v[60:63]
	s_nop 2
	ds_read_b128 v[60:63], v56 offset:256
	ds_read_b128 v[64:67], v56 offset:8448
	ds_read_b128 v[68:71], v56 offset:16640
	ds_read_b128 v[78:81], v56 offset:24832
	v_mfma_f32_16x16x32_f16 v[52:55], v[86:89], v[74:77], v[52:55]
	ds_read_b128 v[82:85], v56 offset:33024
	ds_read_b128 v[86:89], v56 offset:41216
	ds_read_b128 v[90:93], v56 offset:49408
	ds_read_b128 v[94:97], v56 offset:57600
	v_mfma_f32_16x16x32_f16 v[30:33], v[98:101], v[74:77], v[30:33]
	s_waitcnt vmcnt(3) lgkmcnt(7)
	v_mfma_f32_16x16x32_f16 v[12:15], v[60:63], v[20:23], v[12:15]
	ds_read_b128 v[60:63], v57 offset:256
	s_waitcnt lgkmcnt(7)
	v_mfma_f32_16x16x32_f16 v[26:29], v[64:67], v[20:23], v[26:29]
	s_waitcnt lgkmcnt(6)
	v_mfma_f32_16x16x32_f16 v[34:37], v[68:71], v[20:23], v[34:37]
	ds_read_b128 v[64:67], v57 offset:8448
	ds_read_b128 v[68:71], v57 offset:16640
	ds_read_b128 v[74:77], v57 offset:24832
	s_waitcnt lgkmcnt(8)
	v_mfma_f32_16x16x32_f16 v[46:49], v[78:81], v[20:23], v[46:49]
	s_waitcnt lgkmcnt(7)
	v_mfma_f32_16x16x32_f16 v[38:41], v[82:85], v[20:23], v[38:41]
	s_waitcnt lgkmcnt(6)
	v_mfma_f32_16x16x32_f16 v[42:45], v[86:89], v[20:23], v[42:45]
	s_waitcnt lgkmcnt(5)
	v_mfma_f32_16x16x32_f16 v[52:55], v[90:93], v[20:23], v[52:55]
	ds_read_b128 v[78:81], v57 offset:33024
	ds_read_b128 v[82:85], v57 offset:41216
	ds_read_b128 v[86:89], v57 offset:49408
	ds_read_b128 v[90:93], v57 offset:57600
	s_waitcnt lgkmcnt(8)
	v_mfma_f32_16x16x32_f16 v[20:23], v[94:97], v[20:23], v[30:33]
	s_waitcnt vmcnt(2) lgkmcnt(7)
	v_mfma_f32_16x16x32_f16 v[12:15], v[60:63], v[16:19], v[12:15]
	s_waitcnt lgkmcnt(6)
	v_mfma_f32_16x16x32_f16 v[26:29], v[64:67], v[16:19], v[26:29]
	s_waitcnt lgkmcnt(5)
	v_mfma_f32_16x16x32_f16 v[30:33], v[68:71], v[16:19], v[34:37]
	s_waitcnt lgkmcnt(4)
	v_mfma_f32_16x16x32_f16 v[34:37], v[74:77], v[16:19], v[46:49]
	s_nop 2
	ds_read_b128 v[46:49], v6 offset:256
	ds_read_b128 v[60:63], v6 offset:8448
	ds_read_b128 v[64:67], v6 offset:16640
	ds_read_b128 v[68:71], v6 offset:24832
	s_waitcnt lgkmcnt(7)
	v_mfma_f32_16x16x32_f16 v[38:41], v[78:81], v[16:19], v[38:41]
	s_waitcnt lgkmcnt(6)
	v_mfma_f32_16x16x32_f16 v[42:45], v[82:85], v[16:19], v[42:45]
	s_waitcnt lgkmcnt(5)
	v_mfma_f32_16x16x32_f16 v[52:55], v[86:89], v[16:19], v[52:55]
	ds_read_b128 v[74:77], v6 offset:33024
	ds_read_b128 v[78:81], v6 offset:41216
	ds_read_b128 v[82:85], v6 offset:49408
	ds_read_b128 v[86:89], v6 offset:57600
	s_waitcnt lgkmcnt(8)
	v_mfma_f32_16x16x32_f16 v[16:19], v[90:93], v[16:19], v[20:23]
	s_waitcnt vmcnt(1) lgkmcnt(7)
	v_mfma_f32_16x16x32_f16 v[12:15], v[46:49], v[8:11], v[12:15]
	s_waitcnt lgkmcnt(6)
	v_mfma_f32_16x16x32_f16 v[20:23], v[60:63], v[8:11], v[26:29]
	s_waitcnt lgkmcnt(5)
	v_mfma_f32_16x16x32_f16 v[26:29], v[64:67], v[8:11], v[30:33]
	s_waitcnt lgkmcnt(4)
	v_mfma_f32_16x16x32_f16 v[30:33], v[68:71], v[8:11], v[34:37]
	s_waitcnt lgkmcnt(3)
	v_mfma_f32_16x16x32_f16 v[34:37], v[74:77], v[8:11], v[38:41]
	s_waitcnt lgkmcnt(2)
	v_mfma_f32_16x16x32_f16 v[38:41], v[78:81], v[8:11], v[42:45]
	s_nop 2
	ds_read_b128 v[42:45], v7 offset:256
	ds_read_b128 v[46:49], v7 offset:8448
	ds_read_b128 v[60:63], v7 offset:16640
	ds_read_b128 v[64:67], v7 offset:24832
	s_waitcnt lgkmcnt(5)
	v_mfma_f32_16x16x32_f16 v[52:55], v[82:85], v[8:11], v[52:55]
	ds_read_b128 v[68:71], v7 offset:33024
	ds_read_b128 v[74:77], v7 offset:41216
	ds_read_b128 v[78:81], v7 offset:49408
	ds_read_b128 v[82:85], v7 offset:57600
	s_waitcnt lgkmcnt(8)
	v_mfma_f32_16x16x32_f16 v[6:9], v[86:89], v[8:11], v[16:19]
	s_waitcnt vmcnt(0) lgkmcnt(7)
	v_mfma_f32_16x16x32_f16 v[10:13], v[42:45], v[2:5], v[12:15]
	s_waitcnt lgkmcnt(6)
	v_mfma_f32_16x16x32_f16 v[14:17], v[46:49], v[2:5], v[20:23]
	s_waitcnt lgkmcnt(5)
	v_mfma_f32_16x16x32_f16 v[18:21], v[60:63], v[2:5], v[26:29]
	s_waitcnt lgkmcnt(4)
	v_mfma_f32_16x16x32_f16 v[26:29], v[64:67], v[2:5], v[30:33]
	s_waitcnt lgkmcnt(3)
	v_mfma_f32_16x16x32_f16 v[30:33], v[68:71], v[2:5], v[34:37]
	s_waitcnt lgkmcnt(2)
	v_mfma_f32_16x16x32_f16 v[34:37], v[74:77], v[2:5], v[38:41]
	s_waitcnt lgkmcnt(1)
	v_mfma_f32_16x16x32_f16 v[38:41], v[78:81], v[2:5], v[52:55]
	s_waitcnt lgkmcnt(0)
	v_mfma_f32_16x16x32_f16 v[2:5], v[82:85], v[2:5], v[6:9]
	v_lshlrev_b32_e32 v24, 4, v51
	s_nop 1
	v_or_b32_e32 v6, v1, v58
	v_lshl_add_u64 v[22:23], s[8:9], 0, v[24:25]
	v_lshlrev_b32_e32 v25, 2, v6
	ds_write_b128 v0, v[10:13]
	ds_write_b128 v0, v[14:17] offset:64
	ds_write_b128 v0, v[18:21] offset:128
	ds_bpermute_b32 v10, v25, v50
	v_mul_u32_u24_e32 v1, 0x110, v1
	v_add3_u32 v24, v73, v24, v1
	v_or_b32_e32 v1, 16, v25
	ds_bpermute_b32 v14, v1, v50
	ds_write_b128 v0, v[26:29] offset:192
	ds_read_b128 v[6:9], v24
	s_waitcnt lgkmcnt(3)
	v_ashrrev_i32_e32 v11, 31, v10
	v_or_b32_e32 v1, 32, v25
	v_lshlrev_b64 v[10:11], 9, v[10:11]
	ds_bpermute_b32 v18, v1, v50
	v_lshl_add_u64 v[16:17], v[22:23], 0, v[10:11]
	ds_read_b128 v[10:13], v24 offset:1088
	s_waitcnt lgkmcnt(4)
	v_ashrrev_i32_e32 v15, 31, v14
	v_or_b32_e32 v1, 48, v25
	s_waitcnt lgkmcnt(2)
	global_store_dwordx4 v[16:17], v[6:9], off sc1
	s_waitcnt lgkmcnt(1)
	v_ashrrev_i32_e32 v19, 31, v18
	v_lshlrev_b64 v[6:7], 9, v[14:15]
	ds_bpermute_b32 v14, v1, v50
	v_lshl_add_u64 v[20:21], v[22:23], 0, v[6:7]
	ds_read_b128 v[6:9], v24 offset:2176
	s_waitcnt lgkmcnt(2)
	global_store_dwordx4 v[20:21], v[10:13], off sc1
	s_waitcnt lgkmcnt(1)
	v_ashrrev_i32_e32 v15, 31, v14
	v_lshlrev_b64 v[10:11], 9, v[18:19]
	v_lshl_add_u64 v[18:19], v[22:23], 0, v[10:11]
	ds_read_b128 v[10:13], v24 offset:3264
	s_waitcnt lgkmcnt(1)
	global_store_dwordx4 v[18:19], v[6:9], off sc1
	s_nop 1
	v_lshlrev_b64 v[6:7], 9, v[14:15]
	v_lshl_add_u64 v[22:23], v[22:23], 0, v[6:7]
	s_waitcnt lgkmcnt(0)
	global_store_dwordx4 v[22:23], v[10:13], off sc1
	ds_write_b128 v0, v[30:33]
	ds_write_b128 v0, v[34:37] offset:64
	ds_write_b128 v0, v[38:41] offset:128
	ds_write_b128 v0, v[2:5] offset:192
	ds_read_b128 v[0:3], v24
	ds_read_b128 v[4:7], v24 offset:1088
	ds_read_b128 v[8:11], v24 offset:2176
	ds_read_b128 v[12:15], v24 offset:3264
	s_waitcnt lgkmcnt(3)
	global_store_dwordx4 v[16:17], v[0:3], off offset:256 sc1
	s_waitcnt lgkmcnt(2)
	global_store_dwordx4 v[20:21], v[4:7], off offset:256 sc1
	s_waitcnt lgkmcnt(1)
	global_store_dwordx4 v[18:19], v[8:11], off offset:256 sc1
	s_waitcnt lgkmcnt(0)
	global_store_dwordx4 v[22:23], v[12:15], off offset:256 sc1

	.text
	.p2alignl 6, 3212836864
	.fill 256, 4, 3212836864
	.p2alignl 8, 3212836864
